# speedup vs baseline: 1.0097x; 1.0091x over previous
.LBB1_2:
	s_or_b64 exec, exec, s[8:9]
	s_ashr_i32 s9, s2, 3
	s_and_b32 s8, s2, 7
	s_and_b32 s9, s9, -8
	s_bfe_u32 s20, s3, 0x20006
	s_or_b32 s10, s9, s8
	s_lshl_b32 s2, s2, 4
	s_lshr_b32 s22, s3, 6
	v_bfe_u32 v1, v0, 5, 1
	s_and_b32 s2, s2, 0x380
	s_lshl_b32 s8, s20, 5
	s_ashr_i32 s11, s10, 31
	s_or_b32 s2, s8, s2
	s_lshl_b64 s[8:9], s[10:11], 19
	v_lshl_or_b32 v2, s22, 1, v1
	s_waitcnt lgkmcnt(0)
	s_cmpk_gt_u32 s3, 0xff
	s_cselect_b32 s44, s46, s44
	s_cselect_b32 s45, s47, s45
	v_and_b32_e32 v108, 0xff, v0
	v_lshlrev_b32_e32 v108, 2, v108
	global_load_dword v108, v108, s[44:45]
	s_add_u32 s14, s4, s8
	v_lshlrev_b32_e32 v6, 9, v2
	v_lshlrev_b32_e32 v2, 2, v2
	v_and_b32_e32 v5, 31, v0
	s_addc_u32 s15, s5, s9
	v_and_b32_e32 v2, 12, v2
	s_bfe_u32 s4, s3, 0x20007
	v_bitop3_b32 v2, v2, v5, s4 bitop3:0x36
	s_lshl_b32 s4, s22, 10
	v_lshl_or_b32 v192, v2, 4, v6
	s_add_i32 s21, s4, 0
	s_mov_b32 s4, m0
	s_mov_b32 m0, s21
	s_nop 0
	global_load_lds_dwordx4 v192, s[6:7]
	s_mov_b32 m0, s4
	s_add_u32 s4, s6, 0x2000
	s_addc_u32 s5, s7, 0
	s_add_i32 s31, s21, 0x2000
	s_mov_b32 s8, m0
	s_mov_b32 m0, s31
	s_nop 0
	global_load_lds_dwordx4 v192, s[4:5]
	s_mov_b32 m0, s8
	s_add_u32 s4, s6, 0x4000
	s_addc_u32 s5, s7, 0
	s_add_i32 s33, s21, 0x4000
	s_mov_b32 s8, m0
	s_mov_b32 m0, s33
	s_nop 0
	global_load_lds_dwordx4 v192, s[4:5]
	s_mov_b32 m0, s8
	s_add_u32 s4, s6, 0x6000
	s_addc_u32 s5, s7, 0
	s_add_i32 s34, s21, 0x6000
	s_mov_b32 s8, m0
	s_mov_b32 m0, s34
	s_nop 0
	global_load_lds_dwordx4 v192, s[4:5]
	s_mov_b32 m0, s8
	s_add_u32 s4, s6, 0x8000
	s_addc_u32 s5, s7, 0
	s_add_i32 s23, s21, 0x8000
	s_mov_b32 s8, m0
	s_mov_b32 m0, s23
	s_nop 0
	global_load_lds_dwordx4 v192, s[4:5]
	s_mov_b32 m0, s8
	s_add_u32 s4, s6, 0xa000
	s_addc_u32 s5, s7, 0
	s_add_i32 s24, s21, 0xa000
	s_mov_b32 s8, m0
	s_mov_b32 m0, s24
	s_nop 0
	global_load_lds_dwordx4 v192, s[4:5]
	s_mov_b32 m0, s8
	s_add_u32 s4, s6, 0xc000
	s_addc_u32 s5, s7, 0
	s_add_i32 s25, s21, 0xc000
	s_mov_b32 s8, m0
	s_mov_b32 m0, s25
	s_nop 0
	global_load_lds_dwordx4 v192, s[4:5]
	s_mov_b32 m0, s8
	s_add_u32 s4, s6, 0xe000
	s_addc_u32 s5, s7, 0
	s_add_i32 s26, s21, 0xe000
	s_mov_b32 s8, m0
	s_mov_b32 m0, s26
	s_nop 0
	global_load_lds_dwordx4 v192, s[4:5]
	s_mov_b32 m0, s8
	s_and_b32 s4, s2, 0x380
	s_lshl_b32 s4, s4, 9
	s_add_u32 s4, s14, s4
	s_addc_u32 s5, s15, 0
	s_add_i32 s27, s21, 0x10000
	s_add_i32 s28, s21, 0x12000
	s_add_i32 s29, s21, 0x14000
	s_add_i32 s30, s21, 0x16000
	s_mov_b32 s8, m0
	s_mov_b32 m0, s27
	s_nop 0
	global_load_lds_dwordx4 v192, s[4:5]
	s_mov_b32 m0, s8
	s_add_u32 s40, s4, 0x2000
	s_addc_u32 s41, s5, 0
	s_mov_b32 s8, m0
	s_mov_b32 m0, s28
	s_nop 0
	global_load_lds_dwordx4 v192, s[40:41]
	s_mov_b32 m0, s8
	s_add_u32 s40, s4, 0x4000
	s_addc_u32 s41, s5, 0
	s_mov_b32 s8, m0
	s_mov_b32 m0, s29
	s_nop 0
	global_load_lds_dwordx4 v192, s[40:41]
	s_mov_b32 m0, s8
	s_add_u32 s40, s4, 0x6000
	s_addc_u32 s41, s5, 0
	s_mov_b32 s8, m0
	s_mov_b32 m0, s30
	s_nop 0
	global_load_lds_dwordx4 v192, s[40:41]
	s_mov_b32 m0, s8
	s_add_u32 s40, s4, 0x8000
	s_addc_u32 s41, s5, 0
	s_add_i32 s42, s21, 0x18000
	s_mov_b32 s8, m0
	s_mov_b32 m0, s42
	s_nop 0
	global_load_lds_dwordx4 v192, s[40:41]
	s_mov_b32 m0, s8
	s_add_u32 s40, s4, 0xa000
	s_addc_u32 s41, s5, 0
	s_add_i32 s42, s21, 0x1a000
	s_mov_b32 s8, m0
	s_mov_b32 m0, s42
	s_nop 0
	global_load_lds_dwordx4 v192, s[40:41]
	s_mov_b32 m0, s8
	s_add_u32 s40, s4, 0xc000
	s_addc_u32 s41, s5, 0
	s_add_i32 s42, s21, 0x1c000
	s_mov_b32 s8, m0
	s_mov_b32 m0, s42
	s_nop 0
	global_load_lds_dwordx4 v192, s[40:41]
	s_mov_b32 m0, s8
	s_add_u32 s40, s4, 0xe000
	s_addc_u32 s41, s5, 0
	s_add_i32 s42, s21, 0x1e000
	s_mov_b32 s8, m0
	s_mov_b32 m0, s42
	s_nop 0
	global_load_lds_dwordx4 v192, s[40:41]
	s_mov_b32 m0, s8
	s_load_dwordx2 s[8:9], s[0:1], 0x18
	s_load_dwordx2 s[12:13], s[0:1], 0x28
	v_and_b32_e32 v81, 63, v0
	v_lshlrev_b32_e32 v2, 2, v0
	v_add_u32_e32 v6, 0x22000, v2
	s_waitcnt vmcnt(16)
	ds_write_b32 v6, v108
	s_lshr_b32 s5, s3, 8
	s_lshl_b32 s16, s20, 12
	s_lshl_b32 s4, s5, 5
	s_add_i32 s35, s16, 0
	s_add_u32 s18, s6, 0x18000
	v_and_b32_e32 v2, 12, v2
	v_bfe_u32 v0, v0, 2, 2
	s_addc_u32 s19, s7, 0
	v_bitop3_b32 v0, v2, v1, v0 bitop3:0x36
	s_add_u32 s16, s14, 0x8000
	v_lshlrev_b32_e32 v100, 4, v0
	v_or_b32_e32 v0, s4, v5
	s_addc_u32 s17, s15, 0
	s_lshl_b32 s36, s5, 7
	v_lshl_add_u32 v101, v0, 9, 0
	v_lshl_or_b32 v0, v1, 4, s36
	v_add_u32_e32 v0, 0, v0
	v_add_u32_e32 v83, v101, v100
	s_waitcnt vmcnt(0)
	s_waitcnt lgkmcnt(0)
	s_barrier
	s_lshl_b32 s40, s20, 14
	s_add_i32 s40, s40, 0x10000
	v_lshl_add_u32 v108, v5, 9, s40
	v_add_u32_e32 v109, v108, v100
	ds_read_b128 v[68:71], v109
	ds_read_b128 v[76:79], v109 offset:256
	v_xor_b32_e32 v109, 0x20, v100
	v_add_u32_e32 v109, v108, v109
	ds_read_b128 v[60:63], v109
	ds_read_b128 v[72:75], v109 offset:256
	v_xor_b32_e32 v109, 0x40, v100
	v_add_u32_e32 v109, v108, v109
	ds_read_b128 v[52:55], v109
	ds_read_b128 v[64:67], v109 offset:256
	v_xor_b32_e32 v109, 0x60, v100
	v_add_u32_e32 v109, v108, v109
	ds_read_b128 v[48:51], v109
	ds_read_b128 v[56:59], v109 offset:256
	v_xor_b32_e32 v109, 0x80, v100
	v_add_u32_e32 v109, v108, v109
	ds_read_b128 v[36:39], v109
	ds_read_b128 v[44:47], v109 offset:256
	v_xor_b32_e32 v109, 0xa0, v100
	v_add_u32_e32 v109, v108, v109
	ds_read_b128 v[28:31], v109
	ds_read_b128 v[40:43], v109 offset:256
	v_xor_b32_e32 v109, 0xc0, v100
	v_add_u32_e32 v109, v108, v109
	ds_read_b128 v[24:27], v109
	ds_read_b128 v[32:35], v109 offset:256
	v_xor_b32_e32 v109, 0xe0, v100
	v_add_u32_e32 v109, v108, v109
	ds_read_b128 v[20:23], v109
	ds_read_b128 v[16:19], v109 offset:256
	s_waitcnt lgkmcnt(0)
	s_barrier
	s_add_u32 s40, s6, 0x10000
	s_addc_u32 s41, s7, 0
	s_mov_b32 s42, m0
	s_mov_b32 m0, s27
	s_nop 0
	global_load_lds_dwordx4 v192, s[40:41]
	s_mov_b32 m0, s42
	s_add_u32 s40, s6, 0x12000
	s_addc_u32 s41, s7, 0
	s_mov_b32 s42, m0
	s_mov_b32 m0, s28
	s_nop 0
	global_load_lds_dwordx4 v192, s[40:41]
	s_mov_b32 m0, s42
	s_add_u32 s40, s6, 0x14000
	s_addc_u32 s41, s7, 0
	s_mov_b32 s42, m0
	s_mov_b32 m0, s29
	s_nop 0
	global_load_lds_dwordx4 v192, s[40:41]
	s_mov_b32 m0, s42
	s_add_u32 s40, s6, 0x16000
	s_addc_u32 s41, s7, 0
	s_mov_b32 s42, m0
	s_mov_b32 m0, s30
	s_nop 0
	global_load_lds_dwordx4 v192, s[40:41]
	s_mov_b32 m0, s42
	v_add_u32_e32 v80, 0x22000, v0
	v_lshl_add_u32 v81, v81, 4, s35
	v_add_u32_e32 v81, 0x18000, v81
	v_lshl_add_u32 v82, s5, 11, v81
	ds_read_b128 v[0:3], v80 offset:0
	ds_read_b128 v[4:7], v80 offset:32
	ds_read_b128 v[8:11], v80 offset:64
	ds_read_b128 v[12:15], v80 offset:96
	ds_read_b128 v[108:111], v80 offset:256
	ds_read_b128 v[112:115], v80 offset:288
	ds_read_b128 v[116:119], v80 offset:320
	ds_read_b128 v[120:123], v80 offset:352
	v_xor_b32_e32 v84, 0x20, v100
	v_add_u32_e32 v84, v101, v84
	v_xor_b32_e32 v85, 0x40, v100
	v_add_u32_e32 v85, v101, v85
	v_xor_b32_e32 v86, 0x60, v100
	v_add_u32_e32 v86, v101, v86
	v_xor_b32_e32 v87, 0x80, v100
	v_add_u32_e32 v87, v101, v87
	v_xor_b32_e32 v88, 0xa0, v100
	v_add_u32_e32 v88, v101, v88
	v_xor_b32_e32 v89, 0xc0, v100
	v_add_u32_e32 v89, v101, v89
	v_xor_b32_e32 v90, 0xe0, v100
	v_add_u32_e32 v90, v101, v90
	v_add_u32_e32 v208, 0x10000, v83
	v_add_u32_e32 v209, 0x10000, v84
	v_add_u32_e32 v210, 0x10000, v85
	v_add_u32_e32 v211, 0x10000, v86
	v_add_u32_e32 v212, 0x10000, v87
	v_add_u32_e32 v213, 0x10000, v88
	v_add_u32_e32 v214, 0x10000, v89
	v_add_u32_e32 v215, 0x10000, v90
	ds_read_b128 v[92:95], v83
	ds_read_b128 v[96:99], v83 offset:256
	ds_read_b128 v[200:203], v84
	ds_read_b128 v[204:207], v84 offset:256
	s_waitcnt lgkmcnt(8)
	s_waitcnt lgkmcnt(3)
	v_mfma_f32_32x32x16_bf16 v[0:15], v[92:95], v[68:71], v[0:15]
	s_waitcnt lgkmcnt(2)
	v_mfma_f32_32x32x16_bf16 v[0:15], v[96:99], v[76:79], v[0:15]
	ds_read_b128 v[92:95], v85
	ds_read_b128 v[96:99], v85 offset:256
	s_waitcnt lgkmcnt(3)
	v_mfma_f32_32x32x16_bf16 v[0:15], v[200:203], v[60:63], v[0:15]
	s_waitcnt lgkmcnt(2)
	v_mfma_f32_32x32x16_bf16 v[0:15], v[204:207], v[72:75], v[0:15]
	ds_read_b128 v[200:203], v86
	ds_read_b128 v[204:207], v86 offset:256
	s_waitcnt lgkmcnt(3)
	v_mfma_f32_32x32x16_bf16 v[0:15], v[92:95], v[52:55], v[0:15]
	s_waitcnt lgkmcnt(2)
	v_mfma_f32_32x32x16_bf16 v[0:15], v[96:99], v[64:67], v[0:15]
	ds_read_b128 v[92:95], v87
	ds_read_b128 v[96:99], v87 offset:256
	s_waitcnt lgkmcnt(3)
	v_mfma_f32_32x32x16_bf16 v[0:15], v[200:203], v[48:51], v[0:15]
	s_waitcnt lgkmcnt(2)
	v_mfma_f32_32x32x16_bf16 v[0:15], v[204:207], v[56:59], v[0:15]
	ds_read_b128 v[200:203], v88
	ds_read_b128 v[204:207], v88 offset:256
	s_waitcnt lgkmcnt(3)
	v_mfma_f32_32x32x16_bf16 v[0:15], v[92:95], v[36:39], v[0:15]
	s_waitcnt lgkmcnt(2)
	v_mfma_f32_32x32x16_bf16 v[0:15], v[96:99], v[44:47], v[0:15]
	ds_read_b128 v[92:95], v89
	ds_read_b128 v[96:99], v89 offset:256
	s_waitcnt lgkmcnt(3)
	v_mfma_f32_32x32x16_bf16 v[0:15], v[200:203], v[28:31], v[0:15]
	s_waitcnt lgkmcnt(2)
	v_mfma_f32_32x32x16_bf16 v[0:15], v[204:207], v[40:43], v[0:15]
	ds_read_b128 v[200:203], v90
	ds_read_b128 v[204:207], v90 offset:256
	s_waitcnt lgkmcnt(3)
	v_mfma_f32_32x32x16_bf16 v[0:15], v[92:95], v[24:27], v[0:15]
	s_waitcnt lgkmcnt(2)
	v_mfma_f32_32x32x16_bf16 v[0:15], v[96:99], v[32:35], v[0:15]
	ds_read_b128 v[92:95], v83 offset:32768
	ds_read_b128 v[96:99], v83 offset:33024
	s_waitcnt lgkmcnt(3)
	v_mfma_f32_32x32x16_bf16 v[0:15], v[200:203], v[20:23], v[0:15]
	s_waitcnt lgkmcnt(2)
	v_mfma_f32_32x32x16_bf16 v[0:15], v[204:207], v[16:19], v[0:15]
	ds_read_b128 v[200:203], v84 offset:32768
	ds_read_b128 v[204:207], v84 offset:33024
	s_waitcnt lgkmcnt(15)
	s_waitcnt lgkmcnt(3)
	v_mfma_f32_32x32x16_bf16 v[108:123], v[92:95], v[68:71], v[108:123]
	s_waitcnt lgkmcnt(2)
	v_mfma_f32_32x32x16_bf16 v[108:123], v[96:99], v[76:79], v[108:123]
	ds_read_b128 v[92:95], v85 offset:32768
	ds_read_b128 v[96:99], v85 offset:33024
	s_waitcnt lgkmcnt(3)
	v_mfma_f32_32x32x16_bf16 v[108:123], v[200:203], v[60:63], v[108:123]
	s_waitcnt lgkmcnt(2)
	v_mfma_f32_32x32x16_bf16 v[108:123], v[204:207], v[72:75], v[108:123]
	ds_read_b128 v[200:203], v86 offset:32768
	ds_read_b128 v[204:207], v86 offset:33024
	s_nop 1
	v_cvt_pk_bf16_f32 v216, v0, v1
	v_cvt_pk_bf16_f32 v217, v2, v3
	v_cvt_pk_bf16_f32 v218, v4, v5
	v_cvt_pk_bf16_f32 v219, v6, v7
	s_waitcnt lgkmcnt(3)
	v_mfma_f32_32x32x16_bf16 v[108:123], v[92:95], v[52:55], v[108:123]
	s_waitcnt lgkmcnt(2)
	v_mfma_f32_32x32x16_bf16 v[108:123], v[96:99], v[64:67], v[108:123]
	ds_read_b128 v[92:95], v87 offset:32768
	ds_read_b128 v[96:99], v87 offset:33024
	v_cvt_pk_bf16_f32 v220, v8, v9
	v_cvt_pk_bf16_f32 v221, v10, v11
	v_cvt_pk_bf16_f32 v222, v12, v13
	v_cvt_pk_bf16_f32 v223, v14, v15
	ds_write_b128 v82, v[216:219]
	ds_write_b128 v82, v[220:223] offset:1024
	s_waitcnt lgkmcnt(5)
	v_mfma_f32_32x32x16_bf16 v[108:123], v[200:203], v[48:51], v[108:123]
	s_waitcnt lgkmcnt(4)
	v_mfma_f32_32x32x16_bf16 v[108:123], v[204:207], v[56:59], v[108:123]
	ds_read_b128 v[200:203], v88 offset:32768
	ds_read_b128 v[204:207], v88 offset:33024
	s_waitcnt vmcnt(0)
	s_waitcnt lgkmcnt(2)
	s_barrier
	s_add_u32 s40, s6, 0x18000
	s_addc_u32 s41, s7, 0
	s_mov_b32 s42, m0
	s_mov_b32 m0, s21
	s_nop 0
	global_load_lds_dwordx4 v192, s[40:41]
	s_mov_b32 m0, s42
	s_add_u32 s40, s6, 0x1a000
	s_addc_u32 s41, s7, 0
	s_mov_b32 s42, m0
	s_mov_b32 m0, s31
	s_nop 0
	global_load_lds_dwordx4 v192, s[40:41]
	s_mov_b32 m0, s42
	s_waitcnt lgkmcnt(5)
	v_mfma_f32_32x32x16_bf16 v[108:123], v[92:95], v[36:39], v[108:123]
	s_waitcnt lgkmcnt(4)
	v_mfma_f32_32x32x16_bf16 v[108:123], v[96:99], v[44:47], v[108:123]
	ds_read_b128 v[92:95], v89 offset:32768
	ds_read_b128 v[96:99], v89 offset:33024
	s_add_u32 s40, s6, 0x1c000
	s_addc_u32 s41, s7, 0
	s_mov_b32 s42, m0
	s_mov_b32 m0, s33
	s_nop 0
	global_load_lds_dwordx4 v192, s[40:41]
	s_mov_b32 m0, s42
	s_add_u32 s40, s6, 0x1e000
	s_addc_u32 s41, s7, 0
	s_mov_b32 s42, m0
	s_mov_b32 m0, s34
	s_nop 0
	global_load_lds_dwordx4 v192, s[40:41]
	s_mov_b32 m0, s42
	ds_read_b128 v[128:131], v81
	ds_read_b128 v[132:135], v81 offset:1024
	ds_read_b128 v[136:139], v81 offset:2048
	ds_read_b128 v[140:143], v81 offset:3072
	s_waitcnt lgkmcnt(7)
	v_mfma_f32_32x32x16_bf16 v[108:123], v[200:203], v[28:31], v[108:123]
	s_waitcnt lgkmcnt(6)
	v_mfma_f32_32x32x16_bf16 v[108:123], v[204:207], v[40:43], v[108:123]
	ds_read_b128 v[200:203], v90 offset:32768
	ds_read_b128 v[204:207], v90 offset:33024
	ds_read_b128 v[0:3], v80 offset:512
	ds_read_b128 v[4:7], v80 offset:544
	ds_read_b128 v[8:11], v80 offset:576
	ds_read_b128 v[12:15], v80 offset:608
	s_waitcnt lgkmcnt(11)
	v_mfma_f32_32x32x16_bf16 v[108:123], v[92:95], v[24:27], v[108:123]
	s_waitcnt lgkmcnt(10)
	v_mfma_f32_32x32x16_bf16 v[108:123], v[96:99], v[32:35], v[108:123]
	ds_read_b128 v[92:95], v208
	ds_read_b128 v[96:99], v208 offset:256
	s_waitcnt lgkmcnt(7)
	v_mfma_f32_32x32x16_bf16 v[108:123], v[200:203], v[20:23], v[108:123]
	s_waitcnt lgkmcnt(6)
	v_mfma_f32_32x32x16_bf16 v[108:123], v[204:207], v[16:19], v[108:123]
	ds_read_b128 v[200:203], v209
	ds_read_b128 v[204:207], v209 offset:256
	s_waitcnt lgkmcnt(4)
	s_waitcnt lgkmcnt(3)
	v_mfma_f32_32x32x16_bf16 v[0:15], v[92:95], v[68:71], v[0:15]
	s_waitcnt lgkmcnt(2)
	v_mfma_f32_32x32x16_bf16 v[0:15], v[96:99], v[76:79], v[0:15]
	ds_read_b128 v[92:95], v210
	ds_read_b128 v[96:99], v210 offset:256
	s_waitcnt lgkmcnt(3)
	v_mfma_f32_32x32x16_bf16 v[0:15], v[200:203], v[60:63], v[0:15]
	s_waitcnt lgkmcnt(2)
	v_mfma_f32_32x32x16_bf16 v[0:15], v[204:207], v[72:75], v[0:15]
	ds_read_b128 v[200:203], v211
	ds_read_b128 v[204:207], v211 offset:256
	s_nop 1
	v_cvt_pk_bf16_f32 v216, v108, v109
	v_cvt_pk_bf16_f32 v217, v110, v111
	v_cvt_pk_bf16_f32 v218, v112, v113
	v_cvt_pk_bf16_f32 v219, v114, v115
	s_waitcnt lgkmcnt(3)
	v_mfma_f32_32x32x16_bf16 v[0:15], v[92:95], v[52:55], v[0:15]
	s_waitcnt lgkmcnt(2)
	v_mfma_f32_32x32x16_bf16 v[0:15], v[96:99], v[64:67], v[0:15]
	ds_read_b128 v[92:95], v212
	ds_read_b128 v[96:99], v212 offset:256
	v_cvt_pk_bf16_f32 v220, v116, v117
	v_cvt_pk_bf16_f32 v221, v118, v119
	v_cvt_pk_bf16_f32 v222, v120, v121
	v_cvt_pk_bf16_f32 v223, v122, v123
	ds_write_b128 v82, v[216:219] offset:20480
	ds_write_b128 v82, v[220:223] offset:21504
	s_waitcnt lgkmcnt(5)
	v_mfma_f32_32x32x16_bf16 v[0:15], v[200:203], v[48:51], v[0:15]
	s_waitcnt lgkmcnt(4)
	v_mfma_f32_32x32x16_bf16 v[0:15], v[204:207], v[56:59], v[0:15]
	ds_read_b128 v[200:203], v213
	ds_read_b128 v[204:207], v213 offset:256
	s_waitcnt vmcnt(0)
	s_waitcnt lgkmcnt(2)
	s_barrier
	s_add_u32 s40, s14, 0x0
	s_addc_u32 s41, s15, 0
	s_mov_b32 s42, m0
	s_mov_b32 m0, s23
	s_nop 0
	global_load_lds_dwordx4 v192, s[40:41]
	s_mov_b32 m0, s42
	s_add_u32 s40, s14, 0x2000
	s_addc_u32 s41, s15, 0
	s_mov_b32 s42, m0
	s_mov_b32 m0, s24
	s_nop 0
	global_load_lds_dwordx4 v192, s[40:41]
	s_mov_b32 m0, s42
	s_waitcnt lgkmcnt(5)
	v_mfma_f32_32x32x16_bf16 v[0:15], v[92:95], v[36:39], v[0:15]
	s_waitcnt lgkmcnt(4)
	v_mfma_f32_32x32x16_bf16 v[0:15], v[96:99], v[44:47], v[0:15]
	ds_read_b128 v[92:95], v214
	ds_read_b128 v[96:99], v214 offset:256
	s_add_u32 s40, s14, 0x4000
	s_addc_u32 s41, s15, 0
	s_mov_b32 s42, m0
	s_mov_b32 m0, s25
	s_nop 0
	global_load_lds_dwordx4 v192, s[40:41]
	s_mov_b32 m0, s42
	s_add_u32 s40, s14, 0x6000
	s_addc_u32 s41, s15, 0
	s_mov_b32 s42, m0
	s_mov_b32 m0, s26
	s_nop 0
	global_load_lds_dwordx4 v192, s[40:41]
	s_mov_b32 m0, s42
	ds_read_b128 v[144:147], v81 offset:20480
	ds_read_b128 v[148:151], v81 offset:21504
	ds_read_b128 v[152:155], v81 offset:22528
	ds_read_b128 v[156:159], v81 offset:23552
	s_waitcnt lgkmcnt(7)
	v_mfma_f32_32x32x16_bf16 v[0:15], v[200:203], v[28:31], v[0:15]
	s_waitcnt lgkmcnt(6)
	v_mfma_f32_32x32x16_bf16 v[0:15], v[204:207], v[40:43], v[0:15]
	ds_read_b128 v[200:203], v215
	ds_read_b128 v[204:207], v215 offset:256
	ds_read_b128 v[108:111], v80 offset:768
	ds_read_b128 v[112:115], v80 offset:800
	ds_read_b128 v[116:119], v80 offset:832
	ds_read_b128 v[120:123], v80 offset:864
	s_waitcnt lgkmcnt(11)
	v_mfma_f32_32x32x16_bf16 v[0:15], v[92:95], v[24:27], v[0:15]
	s_waitcnt lgkmcnt(10)
	v_mfma_f32_32x32x16_bf16 v[0:15], v[96:99], v[32:35], v[0:15]
	ds_read_b128 v[92:95], v83
	ds_read_b128 v[96:99], v83 offset:256
	s_waitcnt lgkmcnt(7)
	v_mfma_f32_32x32x16_bf16 v[0:15], v[200:203], v[20:23], v[0:15]
	s_waitcnt lgkmcnt(6)
	v_mfma_f32_32x32x16_bf16 v[0:15], v[204:207], v[16:19], v[0:15]
	ds_read_b128 v[200:203], v84
	ds_read_b128 v[204:207], v84 offset:256
	s_waitcnt lgkmcnt(4)
	s_waitcnt lgkmcnt(3)
	v_mfma_f32_32x32x16_bf16 v[108:123], v[92:95], v[68:71], v[108:123]
	s_waitcnt lgkmcnt(2)
	v_mfma_f32_32x32x16_bf16 v[108:123], v[96:99], v[76:79], v[108:123]
	ds_read_b128 v[92:95], v85
	ds_read_b128 v[96:99], v85 offset:256
	s_waitcnt lgkmcnt(3)
	v_mfma_f32_32x32x16_bf16 v[108:123], v[200:203], v[60:63], v[108:123]
	s_waitcnt lgkmcnt(2)
	v_mfma_f32_32x32x16_bf16 v[108:123], v[204:207], v[72:75], v[108:123]
	ds_read_b128 v[200:203], v86
	ds_read_b128 v[204:207], v86 offset:256
	s_nop 1
	v_cvt_pk_bf16_f32 v216, v0, v1
	v_cvt_pk_bf16_f32 v217, v2, v3
	v_cvt_pk_bf16_f32 v218, v4, v5
	v_cvt_pk_bf16_f32 v219, v6, v7
	s_waitcnt lgkmcnt(3)
	v_mfma_f32_32x32x16_bf16 v[108:123], v[92:95], v[52:55], v[108:123]
	s_waitcnt lgkmcnt(2)
	v_mfma_f32_32x32x16_bf16 v[108:123], v[96:99], v[64:67], v[108:123]
	ds_read_b128 v[92:95], v87
	ds_read_b128 v[96:99], v87 offset:256
	v_cvt_pk_bf16_f32 v220, v8, v9
	v_cvt_pk_bf16_f32 v221, v10, v11
	v_cvt_pk_bf16_f32 v222, v12, v13
	v_cvt_pk_bf16_f32 v223, v14, v15
	ds_write_b128 v82, v[216:219]
	ds_write_b128 v82, v[220:223] offset:1024
	s_waitcnt lgkmcnt(5)
	v_mfma_f32_32x32x16_bf16 v[108:123], v[200:203], v[48:51], v[108:123]
	s_waitcnt lgkmcnt(4)
	v_mfma_f32_32x32x16_bf16 v[108:123], v[204:207], v[56:59], v[108:123]
	ds_read_b128 v[200:203], v88
	ds_read_b128 v[204:207], v88 offset:256
	s_waitcnt lgkmcnt(2)
	s_barrier
	s_add_u32 s40, s14, 0x8000
	s_addc_u32 s41, s15, 0
	s_mov_b32 s42, m0
	s_mov_b32 m0, s27
	s_nop 0
	global_load_lds_dwordx4 v192, s[40:41]
	s_mov_b32 m0, s42
	s_add_u32 s40, s14, 0xa000
	s_addc_u32 s41, s15, 0
	s_mov_b32 s42, m0
	s_mov_b32 m0, s28
	s_nop 0
	global_load_lds_dwordx4 v192, s[40:41]
	s_mov_b32 m0, s42
	s_waitcnt lgkmcnt(5)
	v_mfma_f32_32x32x16_bf16 v[108:123], v[92:95], v[36:39], v[108:123]
	s_waitcnt lgkmcnt(4)
	v_mfma_f32_32x32x16_bf16 v[108:123], v[96:99], v[44:47], v[108:123]
	ds_read_b128 v[92:95], v89
	ds_read_b128 v[96:99], v89 offset:256
	s_add_u32 s40, s14, 0xc000
	s_addc_u32 s41, s15, 0
	s_mov_b32 s42, m0
	s_mov_b32 m0, s29
	s_nop 0
	global_load_lds_dwordx4 v192, s[40:41]
	s_mov_b32 m0, s42
	s_add_u32 s40, s14, 0xe000
	s_addc_u32 s41, s15, 0
	s_mov_b32 s42, m0
	s_mov_b32 m0, s30
	s_nop 0
	global_load_lds_dwordx4 v192, s[40:41]
	s_mov_b32 m0, s42
	ds_read_b128 v[160:163], v81
	ds_read_b128 v[164:167], v81 offset:1024
	ds_read_b128 v[168:171], v81 offset:2048
	ds_read_b128 v[172:175], v81 offset:3072
	s_waitcnt lgkmcnt(7)
	v_mfma_f32_32x32x16_bf16 v[108:123], v[200:203], v[28:31], v[108:123]
	s_waitcnt lgkmcnt(6)
	v_mfma_f32_32x32x16_bf16 v[108:123], v[204:207], v[40:43], v[108:123]
	ds_read_b128 v[200:203], v90
	ds_read_b128 v[204:207], v90 offset:256
	s_waitcnt lgkmcnt(7)
	v_mfma_f32_32x32x16_bf16 v[108:123], v[92:95], v[24:27], v[108:123]
	s_waitcnt lgkmcnt(6)
	v_mfma_f32_32x32x16_bf16 v[108:123], v[96:99], v[32:35], v[108:123]
	s_waitcnt lgkmcnt(1)
	v_mfma_f32_32x32x16_bf16 v[108:123], v[200:203], v[20:23], v[108:123]
	s_waitcnt lgkmcnt(0)
	v_mfma_f32_32x32x16_bf16 v[108:123], v[204:207], v[16:19], v[108:123]
	s_nop 11
	s_nop 2
	v_cvt_pk_bf16_f32 v216, v108, v109
	v_cvt_pk_bf16_f32 v217, v110, v111
	v_cvt_pk_bf16_f32 v218, v112, v113
	v_cvt_pk_bf16_f32 v219, v114, v115
	v_cvt_pk_bf16_f32 v220, v116, v117
	v_cvt_pk_bf16_f32 v221, v118, v119
	v_cvt_pk_bf16_f32 v222, v120, v121
	v_cvt_pk_bf16_f32 v223, v122, v123
	ds_write_b128 v82, v[216:219] offset:20480
	ds_write_b128 v82, v[220:223] offset:21504
	v_mbcnt_lo_u32_b32 v224, -1, 0
	v_mbcnt_hi_u32_b32 v193, -1, v224
	v_mov_b32_e32 v194, v193
	s_waitcnt vmcnt(4) lgkmcnt(0)
	s_barrier
	ds_read_b128 v[176:179], v81 offset:20480
	ds_read_b128 v[180:183], v81 offset:21504
	ds_read_b128 v[184:187], v81 offset:22528
	ds_read_b128 v[188:191], v81 offset:23552
	s_movk_i32 s7, 0x80
	s_movk_i32 s6, 0xc0
	s_mov_b32 s5, 0x10000
	s_waitcnt lgkmcnt(0)
	s_barrier
	s_cmpk_gt_u32 s3, 0xff
	s_nop 0
	v_and_b32_e32 v196, 31, v194
	v_ashrrev_i32_e32 v197, 5, v194
	v_lshlrev_b32_e32 v195, 2, v194
	v_bfe_u32 v198, v194, 2, 2
	s_cbranch_scc0 .LBB1_16
	v_lshl_add_u32 v0, s20, 2, v197
	v_lshlrev_b32_e32 v3, 2, v197
	v_add_u32_e32 v1, 2, v0
	v_lshlrev_b32_e32 v2, 9, v0
	v_and_b32_e32 v3, 12, v3
	v_bfe_u32 v0, v0, 2, 2
	v_bitop3_b32 v0, v0, v196, v3 bitop3:0x36
	v_lshl_or_b32 v199, v0, 4, v2
	v_lshlrev_b32_e32 v0, 2, v1
	s_bfe_u32 s18, s3, 0x10006
	v_and_b32_e32 v0, 12, v0
	v_bfe_u32 v2, v1, 2, 2
	v_bitop3_b32 v0, v0, v196, v2 bitop3:0x36
	v_lshrrev_b32_e32 v2, 3, v194
	s_lshl_b32 s16, s18, 8
	v_and_b32_e32 v2, 2, v2
	v_bfe_u32 v3, v194, 1, 1
	s_add_i32 s16, s16, 0
	v_lshlrev_b32_e32 v4, 3, v194
	v_lshl_add_u32 v5, v197, 11, s16
	v_bitop3_b32 v2, v2, v197, v3 bitop3:0x36
	v_and_or_b32 v4, v4, 8, v5
	v_lshlrev_b32_e32 v2, 4, v2
	v_lshlrev_b32_e32 v3, 6, v198
	v_lshl_add_u32 v4, v198, 9, v4
	v_or_b32_e32 v5, v2, v3
	v_add_u32_e32 v200, v4, v5
	v_bitop3_b32 v5, v2, v3, 32 bitop3:0xde
	v_add_u32_e32 v6, 0x1000, v4
	v_add_u32_e32 v201, v6, v5
	v_xor_b32_e32 v5, 64, v3
	v_bitop3_b32 v5, v2, v5, 32 bitop3:0xde
	v_add_u32_e32 v203, v6, v5
	v_xor_b32_e32 v5, 0x80, v3
	v_bitop3_b32 v7, v2, v3, 64 bitop3:0xf6
	v_bitop3_b32 v5, v2, v5, 32 bitop3:0xde
	v_add_u32_e32 v202, v4, v7
	v_bitop3_b32 v7, v2, v3, s7 bitop3:0xf6
	v_add_u32_e32 v205, v6, v5
	v_xor_b32_e32 v5, 0xc0, v3
	v_bitop3_b32 v3, v2, v3, s6 bitop3:0xf6
	s_and_b32 s6, s22, 2
	v_lshlrev_b32_e32 v1, 9, v1
	s_lshl_b32 s27, s6, 2
	s_lshl_b32 s7, s6, 8
	s_lshl_b32 s6, s6, 12
	v_lshl_or_b32 v208, v0, 4, v1
	s_lshl_b32 s19, s20, 11
	s_add_i32 s7, s7, 0
	s_add_i32 s6, s6, 0
	v_mov_b32_e32 v0, 0
	v_bitop3_b32 v2, v2, v5, 32 bitop3:0xde
	s_waitcnt vmcnt(0)
	s_add_i32 s19, s19, 0
	s_add_i32 s16, s7, 0x20000
	s_add_i32 s7, s7, 0x20100
	v_lshlrev_b32_e32 v209, 4, v194
	s_add_i32 s6, s6, 0x18000
	v_mov_b32_e32 v14, v0
	v_mov_b32_e32 v15, v0
	v_add_u32_e32 v204, v4, v7
	v_add_u32_e32 v206, v4, v3
	v_add_u32_e32 v207, v6, v2
	v_add_u32_e32 v212, s6, v209
	s_add_u32 s6, s8, 0xfff90000
	v_mov_b32_e32 v1, v0
	v_mov_b32_e32 v2, v0
	v_mov_b32_e32 v3, v0
	v_mov_b32_e32 v4, v0
	v_mov_b32_e32 v5, v0
	v_mov_b32_e32 v6, v0
	v_mov_b32_e32 v7, v0
	v_mov_b32_e32 v8, v0
	v_mov_b32_e32 v9, v0
	v_mov_b32_e32 v10, v0
	v_mov_b32_e32 v11, v0
	v_mov_b32_e32 v12, v0
	v_mov_b32_e32 v13, v0
	v_mov_b64_e32 v[62:63], v[14:15]
	v_mov_b64_e32 v[94:95], v[14:15]
	v_mov_b64_e32 v[126:127], v[14:15]
	v_mov_b64_e32 v[30:31], v[14:15]
	v_mov_b64_e32 v[46:47], v[14:15]
	v_mov_b64_e32 v[78:79], v[14:15]
	v_mov_b64_e32 v[110:111], v[14:15]
	v_add_u32_e32 v210, s16, v195
	v_add_u32_e32 v211, s7, v195
	s_addc_u32 s7, s9, -1
	s_mov_b32 s33, 1
	s_mov_b32 s31, 0x8000
	s_mov_b32 s29, 0x10000
	v_mov_b64_e32 v[60:61], v[12:13]
	v_mov_b64_e32 v[58:59], v[10:11]
	v_mov_b64_e32 v[56:57], v[8:9]
	v_mov_b64_e32 v[54:55], v[6:7]
	v_mov_b64_e32 v[52:53], v[4:5]
	v_mov_b64_e32 v[50:51], v[2:3]
	v_mov_b64_e32 v[48:49], v[0:1]
	v_mov_b64_e32 v[92:93], v[12:13]
	v_mov_b64_e32 v[90:91], v[10:11]
	v_mov_b64_e32 v[88:89], v[8:9]
	v_mov_b64_e32 v[86:87], v[6:7]
	v_mov_b64_e32 v[84:85], v[4:5]
	v_mov_b64_e32 v[82:83], v[2:3]
	v_mov_b64_e32 v[80:81], v[0:1]
	v_mov_b64_e32 v[124:125], v[12:13]
	v_mov_b64_e32 v[122:123], v[10:11]
	v_mov_b64_e32 v[120:121], v[8:9]
	v_mov_b64_e32 v[118:119], v[6:7]
	v_mov_b64_e32 v[116:117], v[4:5]
	v_mov_b64_e32 v[114:115], v[2:3]
	v_mov_b64_e32 v[112:113], v[0:1]
	v_mov_b64_e32 v[28:29], v[12:13]
	v_mov_b64_e32 v[26:27], v[10:11]
	v_mov_b64_e32 v[24:25], v[8:9]
	v_mov_b64_e32 v[22:23], v[6:7]
	v_mov_b64_e32 v[20:21], v[4:5]
	v_mov_b64_e32 v[18:19], v[2:3]
	v_mov_b64_e32 v[16:17], v[0:1]
	v_mov_b64_e32 v[44:45], v[12:13]
	v_mov_b64_e32 v[42:43], v[10:11]
	v_mov_b64_e32 v[40:41], v[8:9]
	v_mov_b64_e32 v[38:39], v[6:7]
	v_mov_b64_e32 v[36:37], v[4:5]
	v_mov_b64_e32 v[34:35], v[2:3]
	v_mov_b64_e32 v[32:33], v[0:1]
	v_mov_b64_e32 v[76:77], v[12:13]
	v_mov_b64_e32 v[74:75], v[10:11]
	v_mov_b64_e32 v[72:73], v[8:9]
	v_mov_b64_e32 v[70:71], v[6:7]
	v_mov_b64_e32 v[68:69], v[4:5]
	v_mov_b64_e32 v[66:67], v[2:3]
	v_mov_b64_e32 v[64:65], v[0:1]
	v_mov_b64_e32 v[108:109], v[12:13]
	v_mov_b64_e32 v[106:107], v[10:11]
	v_mov_b64_e32 v[104:105], v[8:9]
	v_mov_b64_e32 v[102:103], v[6:7]
	v_mov_b64_e32 v[100:101], v[4:5]
	v_mov_b64_e32 v[98:99], v[2:3]
	v_mov_b64_e32 v[96:97], v[0:1]
	s_waitcnt lgkmcnt(0)
	s_barrier
